# rowsum via VALU adds instead of ones-MFMA, diff attention only
# speedup vs baseline: 1.0173x; 1.0173x over previous
; #define MFMA32(a, b, c) __builtin_amdgcn_mfma_f32_32x32x16_bf16((a), (b), (c), 0, 0, 0)
; template <int OFF> DI s16x4 at_tr_read(int vb) { s16x4 r; asm volatile("ds_read_b64_tr_b16 %0, %1 offset:%2" : "=&v"(r) : "v"(vb), "i"(OFF) : "memory"); return r; }
; DI unsigned at_cvtpk(float lo, float hi) { unsigned r; asm volatile("v_cvt_pk_bf16_f32 %0, %1, %2" : "=v"(r) : "v"(lo), "v"(hi)); return r; }
; DI float at_softmax(f32x16& p0, f32x16& p1, float& m_run, bool first, bool nearb, LAS const float* tabp, int lane) {
;     ...
; #pragma unroll
;     for (int i = 0; i < 16; ++i) p0[i] = __builtin_amdgcn_exp2f(p0[i]);
; #pragma unroll
;     for (int i = 0; i < 16; ++i) p1[i] = __builtin_amdgcn_exp2f(p1[i]);
;     return alpha;
; }
; DI bf16x8 at_pack(const f32x16& p, int s8) {
;     u32x4 w; w.x = at_cvtpk(p[s8], p[s8 + 1]); w.y = at_cvtpk(p[s8 + 2], p[s8 + 3]); w.z = at_cvtpk(p[s8 + 4], p[s8 + 5]); w.w = at_cvtpk(p[s8 + 6], p[s8 + 7]);
;     return __builtin_bit_cast(bf16x8, w);
; }
; template <int D0> DI void at_pv_block(f32x16 (&o)[4], int vb, const bf16x8 (&pf)[4]) {
;     const s16x4 l0 = at_tr_read<D0 * 512 + 0 * 4096>(vb), h0 = at_tr_read<D0 * 512 + 0 * 4096 + 2048>(vb), l1 = at_tr_read<D0 * 512 + 1 * 4096>(vb), h1 = at_tr_read<D0 * 512 + 1 * 4096 + 2048>(vb);
;     const s16x4 l2 = at_tr_read<D0 * 512 + 2 * 4096>(vb), h2 = at_tr_read<D0 * 512 + 2 * 4096 + 2048>(vb), l3 = at_tr_read<D0 * 512 + 3 * 4096>(vb), h3 = at_tr_read<D0 * 512 + 3 * 4096 + 2048>(vb);
;     asm volatile("s_waitcnt lgkmcnt(0)" ::: "memory"); __builtin_amdgcn_sched_barrier(0);
;     ...
;     o[D0] = MFMA32(AT_PK(l0, h0), pf[0], o[D0]); o[D0] = MFMA32(AT_PK(l1, h1), pf[1], o[D0]); o[D0] = MFMA32(AT_PK(l2, h2), pf[2], o[D0]); o[D0] = MFMA32(AT_PK(l3, h3), pf[3], o[D0]);
; DI void attn_unit_diff(const Ctx& C, int l, int b, int h, int j) {
;     ...
;             bf16x8 pf[4];
;             pf[0] = at_pack(p0, 0); pf[1] = at_pack(p0, 8); pf[2] = at_pack(p1, 0); pf[3] = at_pack(p1, 8);
;             ol = MFMA32(ones, pf[0], ol); ol = MFMA32(ones, pf[1], ol); ol = MFMA32(ones, pf[2], ol); ol = MFMA32(ones, pf[3], ol);
;             at_pv_block<0>(o, vb, pf); at_pv_block<1>(o, vb, pf); at_pv_block<2>(o, vb, pf); at_pv_block<3>(o, vb, pf);
.LBB0_801:
	v_exp_f32_e32 v2, v113
	v_exp_f32_e32 v6, v117
	v_exp_f32_e32 v7, v118
	v_exp_f32_e32 v8, v119
	v_exp_f32_e32 v9, v120
	v_exp_f32_e32 v10, v121
	v_exp_f32_e32 v11, v122
	v_exp_f32_e32 v12, v123
	v_exp_f32_e32 v13, v124
	v_exp_f32_e32 v113, v96
	v_exp_f32_e32 v100, v100
	v_exp_f32_e32 v101, v101
	v_exp_f32_e32 v102, v102
	v_exp_f32_e32 v103, v103
	v_subrev_u32_e32 v96, s57, v160
	s_mov_b32 s58, s56
	s_mov_b32 s59, s56
	v_exp_f32_e32 v0, v112
	v_exp_f32_e32 v3, v114
	v_exp_f32_e32 v4, v115
	v_exp_f32_e32 v5, v116
	v_exp_f32_e32 v14, v125
	v_exp_f32_e32 v15, v126
	v_exp_f32_e32 v112, v127
	v_exp_f32_e32 v114, v97
	v_exp_f32_e32 v115, v98
	v_exp_f32_e32 v116, v99
	v_add_u32_e32 v117, s49, v96
	v_add_f32_e32 v81, v0, v2
	v_add_f32_e32 v82, v3, v4
	v_add_f32_e32 v83, v5, v6
	v_add_f32_e32 v84, v7, v8
	v_add_f32_e32 v85, v9, v10
	v_add_f32_e32 v86, v11, v12
	v_add_f32_e32 v87, v13, v14
	v_add_f32_e32 v88, v15, v112
	v_add_f32_e32 v89, v113, v114
	v_add_f32_e32 v90, v115, v116
	v_add_f32_e32 v91, v100, v101
	v_add_f32_e32 v92, v102, v103
	v_add_f32_e32 v81, v81, v82
	v_add_f32_e32 v83, v83, v84
	v_add_f32_e32 v85, v85, v86
	v_add_f32_e32 v87, v87, v88
	v_add_f32_e32 v89, v89, v90
	v_add_f32_e32 v91, v91, v92
	v_add_f32_e32 v81, v81, v83
	v_add_f32_e32 v85, v85, v87
	v_add_f32_e32 v89, v89, v91
	v_add_f32_e32 v81, v81, v85
	v_add_f32_e32 v81, v81, v89
	v_cvt_pk_bf16_f32 v96, v0, v2
	v_cvt_pk_bf16_f32 v97, v3, v4
	v_cvt_pk_bf16_f32 v98, v5, v6
	v_cvt_pk_bf16_f32 v99, v7, v8
	v_cvt_pk_bf16_f32 v10, v9, v10
	v_cvt_pk_bf16_f32 v11, v11, v12
	v_cvt_pk_bf16_f32 v12, v13, v14
	v_cvt_pk_bf16_f32 v13, v15, v112
	v_cvt_pk_bf16_f32 v6, v113, v114
	v_cvt_pk_bf16_f32 v7, v115, v116
	v_cvt_pk_bf16_f32 v8, v100, v101
	v_cvt_pk_bf16_f32 v9, v102, v103
	s_mov_b32 s57, s56
	v_exp_f32_e32 v104, v104
	v_exp_f32_e32 v105, v105
	v_exp_f32_e32 v106, v106
	v_exp_f32_e32 v107, v107
	v_exp_f32_e32 v108, v108
	v_exp_f32_e32 v109, v109
	v_exp_f32_e32 v110, v110
	v_exp_f32_e32 v111, v111
	v_cvt_pk_bf16_f32 v2, v104, v105
	v_cvt_pk_bf16_f32 v3, v106, v107
	v_cvt_pk_bf16_f32 v4, v108, v109
	v_cvt_pk_bf16_f32 v5, v110, v111
	v_add_f32_e32 v82, v104, v105
	v_add_f32_e32 v83, v106, v107
	v_add_f32_e32 v84, v108, v109
	v_add_f32_e32 v85, v110, v111
	v_add_f32_e32 v82, v82, v83
	v_add_f32_e32 v84, v84, v85
	v_add_f32_e32 v82, v82, v84
	v_add_f32_e32 v81, v81, v82
	v_add_f32_e32 v80, v80, v81
	ds_read_b64_tr_b16 v[100:101], v117 offset:0
	ds_read_b64_tr_b16 v[102:103], v117 offset:0x800
	ds_read_b64_tr_b16 v[104:105], v117 offset:0x1000
	ds_read_b64_tr_b16 v[106:107], v117 offset:0x1800
	ds_read_b64_tr_b16 v[108:109], v117 offset:0x2000
	ds_read_b64_tr_b16 v[110:111], v117 offset:0x2800
	ds_read_b64_tr_b16 v[112:113], v117 offset:0x3000
	ds_read_b64_tr_b16 v[114:115], v117 offset:0x3800
	s_waitcnt lgkmcnt(0)
	s_nop 0
	v_mfma_f32_32x32x16_bf16 v[64:79], v[100:103], v[96:99], v[64:79]
	ds_read_b64_tr_b16 v[100:101], v117 offset:0x200
	ds_read_b64_tr_b16 v[102:103], v117 offset:0xa00
	v_mfma_f32_32x32x16_bf16 v[64:79], v[104:107], v[10:13], v[64:79]
	ds_read_b64_tr_b16 v[104:105], v117 offset:0x1200
	ds_read_b64_tr_b16 v[106:107], v117 offset:0x1a00
	v_mfma_f32_32x32x16_bf16 v[64:79], v[108:111], v[6:9], v[64:79]
	ds_read_b64_tr_b16 v[108:109], v117 offset:0x2200
	ds_read_b64_tr_b16 v[110:111], v117 offset:0x2a00
	v_mfma_f32_32x32x16_bf16 v[64:79], v[112:115], v[2:5], v[64:79]
	ds_read_b64_tr_b16 v[112:113], v117 offset:0x3200
	ds_read_b64_tr_b16 v[114:115], v117 offset:0x3a00
	s_waitcnt lgkmcnt(0)
	v_mfma_f32_32x32x16_bf16 v[48:63], v[100:103], v[96:99], v[48:63]
	ds_read_b64_tr_b16 v[100:101], v117 offset:0x400
	ds_read_b64_tr_b16 v[102:103], v117 offset:0xc00
	v_mfma_f32_32x32x16_bf16 v[48:63], v[104:107], v[10:13], v[48:63]
	ds_read_b64_tr_b16 v[104:105], v117 offset:0x1400
	ds_read_b64_tr_b16 v[106:107], v117 offset:0x1c00
	v_mfma_f32_32x32x16_bf16 v[48:63], v[108:111], v[6:9], v[48:63]
	ds_read_b64_tr_b16 v[108:109], v117 offset:0x2400
	ds_read_b64_tr_b16 v[110:111], v117 offset:0x2c00
	v_mfma_f32_32x32x16_bf16 v[48:63], v[112:115], v[2:5], v[48:63]
	ds_read_b64_tr_b16 v[112:113], v117 offset:0x3400
	ds_read_b64_tr_b16 v[114:115], v117 offset:0x3c00
	s_waitcnt lgkmcnt(0)
	v_mfma_f32_32x32x16_bf16 v[32:47], v[100:103], v[96:99], v[32:47]
	ds_read_b64_tr_b16 v[100:101], v117 offset:0x600
	ds_read_b64_tr_b16 v[102:103], v117 offset:0xe00
	v_mfma_f32_32x32x16_bf16 v[32:47], v[104:107], v[10:13], v[32:47]
	ds_read_b64_tr_b16 v[104:105], v117 offset:0x1600
	ds_read_b64_tr_b16 v[106:107], v117 offset:0x1e00
	v_mfma_f32_32x32x16_bf16 v[32:47], v[108:111], v[6:9], v[32:47]
	ds_read_b64_tr_b16 v[108:109], v117 offset:0x2600
	ds_read_b64_tr_b16 v[110:111], v117 offset:0x2e00
	v_mfma_f32_32x32x16_bf16 v[32:47], v[112:115], v[2:5], v[32:47]
	ds_read_b64_tr_b16 v[112:113], v117 offset:0x3600
	ds_read_b64_tr_b16 v[114:115], v117 offset:0x3e00
	s_waitcnt lgkmcnt(0)
	v_mfma_f32_32x32x16_bf16 v[16:31], v[100:103], v[96:99], v[16:31]
	s_mov_b64 s[38:39], 0
	v_mfma_f32_32x32x16_bf16 v[16:31], v[104:107], v[10:13], v[16:31]
	v_mfma_f32_32x32x16_bf16 v[16:31], v[108:111], v[6:9], v[16:31]
	v_mfma_f32_32x32x16_bf16 v[16:31], v[112:115], v[2:5], v[16:31]
	s_mov_b64 s[58:59], -1
	s_and_b64 vcc, exec, s[40:41]
	s_cbranch_vccz .LBB0_790

; #define LAS __attribute__((address_space(3)))
; #define CIN(i) ((const float*)*(const GAS float* const __attribute__((address_space(4)))*)(C.ka + 8 * (i)))
; DI void attn_unit_diff(const Ctx& C, int l, int b, int h, int j) {
;     ...
;     const float inv = 1.f / ol[0];
;     LAS float* cmb = (LAS float*)C.lds + (size_t)wq * (64 * 64);
;     f32x4 sgv[4][4];
;     if (g == 0) { const float* sg0 = CIN(I_SUBLN) + l * 128;
; #pragma unroll
;         for (int d0 = 0; d0 < 4; ++d0)
; #pragma unroll
;             for (int gq = 0; gq < 4; ++gq) sgv[d0][gq] = *(const f32x4*)(sg0 + 32 * d0 + 8 * gq + 4 * hi); }
.LBB0_805:
v_lshlrev_b32_e32 v81, 2, v154
v_xor_b32_e32 v81, 0x80, v81
ds_bpermute_b32 v82, v81, v80
s_waitcnt lgkmcnt(0)
v_add_f32_e32 v80, v80, v82
	v_readlane_b32 s38, v252, 27
	v_readlane_b32 s39, v252, 28
	s_and_b64 vcc, s[38:39], exec
	s_cbranch_vccz .LBB0_807
	s_load_dwordx2 s[38:39], s[0:1], 0x38
	v_readlane_b32 s40, v254, 25
	v_readlane_b32 s41, v254, 26
	s_lshl_b64 s[40:41], s[40:41], 2
	v_lshlrev_b32_e32 v2, 2, v156
	s_waitcnt lgkmcnt(0)
	s_add_u32 s38, s38, s40
	v_ashrrev_i32_e32 v3, 31, v2
	s_addc_u32 s39, s39, s41
	v_lshl_add_u64 v[2:3], v[2:3], 2, s[38:39]
	global_load_dwordx4 v[126:129], v[2:3], off
	global_load_dwordx4 v[94:97], v[2:3], off offset:32
	global_load_dwordx4 v[86:89], v[2:3], off offset:64
	global_load_dwordx4 v[82:85], v[2:3], off offset:96
	global_load_dwordx4 v[90:93], v[2:3], off offset:128
	global_load_dwordx4 v[98:101], v[2:3], off offset:160
	global_load_dwordx4 v[102:105], v[2:3], off offset:192
	global_load_dwordx4 v[106:109], v[2:3], off offset:224
	global_load_dwordx4 v[110:113], v[2:3], off offset:256
	global_load_dwordx4 v[114:117], v[2:3], off offset:288
	global_load_dwordx4 v[118:121], v[2:3], off offset:320
	global_load_dwordx4 v[122:125], v[2:3], off offset:352
	global_load_dwordx4 v[130:133], v[2:3], off offset:384
	global_load_dwordx4 v[10:13], v[2:3], off offset:416
	global_load_dwordx4 v[6:9], v[2:3], off offset:448
	s_nop 0
	global_load_dwordx4 v[2:5], v[2:3], off offset:480

; #define MFMA32(a, b, c) __builtin_amdgcn_mfma_f32_32x32x16_bf16((a), (b), (c), 0, 0, 0)
; template <int OFF> DI s16x4 at_tr_read(int vb) { s16x4 r; asm volatile("ds_read_b64_tr_b16 %0, %1 offset:%2" : "=&v"(r) : "v"(vb), "i"(OFF) : "memory"); return r; }
; DI unsigned at_cvtpk(float lo, float hi) { unsigned r; asm volatile("v_cvt_pk_bf16_f32 %0, %1, %2" : "=v"(r) : "v"(lo), "v"(hi)); return r; }
; DI float at_softmax(f32x16& p0, f32x16& p1, float& m_run, bool first, bool nearb, LAS const float* tabp, int lane) {
;     ...
; #pragma unroll
;     for (int i = 0; i < 16; ++i) p0[i] = __builtin_amdgcn_exp2f(p0[i]);
; #pragma unroll
;     for (int i = 0; i < 16; ++i) p1[i] = __builtin_amdgcn_exp2f(p1[i]);
;     return alpha;
; }
; DI bf16x8 at_pack(const f32x16& p, int s8) {
;     u32x4 w; w.x = at_cvtpk(p[s8], p[s8 + 1]); w.y = at_cvtpk(p[s8 + 2], p[s8 + 3]); w.z = at_cvtpk(p[s8 + 4], p[s8 + 5]); w.w = at_cvtpk(p[s8 + 6], p[s8 + 7]);
;     return __builtin_bit_cast(bf16x8, w);
; }
; template <int D0> DI void at_pv_block(f32x16 (&o)[4], int vb, const bf16x8 (&pf)[4]) {
;     const s16x4 l0 = at_tr_read<D0 * 512 + 0 * 4096>(vb), h0 = at_tr_read<D0 * 512 + 0 * 4096 + 2048>(vb), l1 = at_tr_read<D0 * 512 + 1 * 4096>(vb), h1 = at_tr_read<D0 * 512 + 1 * 4096 + 2048>(vb);
;     const s16x4 l2 = at_tr_read<D0 * 512 + 2 * 4096>(vb), h2 = at_tr_read<D0 * 512 + 2 * 4096 + 2048>(vb), l3 = at_tr_read<D0 * 512 + 3 * 4096>(vb), h3 = at_tr_read<D0 * 512 + 3 * 4096 + 2048>(vb);
;     asm volatile("s_waitcnt lgkmcnt(0)" ::: "memory"); __builtin_amdgcn_sched_barrier(0);
;     ...
;     o[D0] = MFMA32(AT_PK(l0, h0), pf[0], o[D0]); o[D0] = MFMA32(AT_PK(l1, h1), pf[1], o[D0]); o[D0] = MFMA32(AT_PK(l2, h2), pf[2], o[D0]); o[D0] = MFMA32(AT_PK(l3, h3), pf[3], o[D0]);
; DI void attn_unit_diff(const Ctx& C, int l, int b, int h, int j) {
;     ...
;             bf16x8 pf[4];
;             pf[0] = at_pack(p0, 0); pf[1] = at_pack(p0, 8); pf[2] = at_pack(p1, 0); pf[3] = at_pack(p1, 8);
;             ol = MFMA32(ones, pf[0], ol); ol = MFMA32(ones, pf[1], ol); ol = MFMA32(ones, pf[2], ol); ol = MFMA32(ones, pf[3], ol);
;             at_pv_block<0>(o, vb, pf); at_pv_block<1>(o, vb, pf); at_pv_block<2>(o, vb, pf); at_pv_block<3>(o, vb, pf);
.LBB0_844:
	v_exp_f32_e32 v2, v113
	v_exp_f32_e32 v6, v117
	v_exp_f32_e32 v7, v118
	v_exp_f32_e32 v8, v119
	v_exp_f32_e32 v9, v120
	v_exp_f32_e32 v10, v121
	v_exp_f32_e32 v11, v122
	v_exp_f32_e32 v12, v123
	v_exp_f32_e32 v13, v124
	v_exp_f32_e32 v113, v96
	v_exp_f32_e32 v100, v100
	v_exp_f32_e32 v101, v101
	v_exp_f32_e32 v102, v102
	v_exp_f32_e32 v103, v103
	v_subrev_u32_e32 v96, s48, v160
	s_mov_b32 s58, s56
	s_mov_b32 s59, s56
	v_exp_f32_e32 v0, v112
	v_exp_f32_e32 v3, v114
	v_exp_f32_e32 v4, v115
	v_exp_f32_e32 v5, v116
	v_exp_f32_e32 v14, v125
	v_exp_f32_e32 v15, v126
	v_exp_f32_e32 v112, v127
	v_exp_f32_e32 v114, v97
	v_exp_f32_e32 v115, v98
	v_exp_f32_e32 v116, v99
	v_add_u32_e32 v117, s31, v96
	v_add_f32_e32 v81, v0, v2
	v_add_f32_e32 v82, v3, v4
	v_add_f32_e32 v83, v5, v6
	v_add_f32_e32 v84, v7, v8
	v_add_f32_e32 v85, v9, v10
	v_add_f32_e32 v86, v11, v12
	v_add_f32_e32 v87, v13, v14
	v_add_f32_e32 v88, v15, v112
	v_add_f32_e32 v89, v113, v114
	v_add_f32_e32 v90, v115, v116
	v_add_f32_e32 v91, v100, v101
	v_add_f32_e32 v92, v102, v103
	v_add_f32_e32 v81, v81, v82
	v_add_f32_e32 v83, v83, v84
	v_add_f32_e32 v85, v85, v86
	v_add_f32_e32 v87, v87, v88
	v_add_f32_e32 v89, v89, v90
	v_add_f32_e32 v91, v91, v92
	v_add_f32_e32 v81, v81, v83
	v_add_f32_e32 v85, v85, v87
	v_add_f32_e32 v89, v89, v91
	v_add_f32_e32 v81, v81, v85
	v_add_f32_e32 v81, v81, v89
	v_cvt_pk_bf16_f32 v96, v0, v2
	v_cvt_pk_bf16_f32 v97, v3, v4
	v_cvt_pk_bf16_f32 v98, v5, v6
	v_cvt_pk_bf16_f32 v99, v7, v8
	v_cvt_pk_bf16_f32 v10, v9, v10
	v_cvt_pk_bf16_f32 v11, v11, v12
	v_cvt_pk_bf16_f32 v12, v13, v14
	v_cvt_pk_bf16_f32 v13, v15, v112
	v_cvt_pk_bf16_f32 v6, v113, v114
	v_cvt_pk_bf16_f32 v7, v115, v116
	v_cvt_pk_bf16_f32 v8, v100, v101
	v_cvt_pk_bf16_f32 v9, v102, v103
	s_mov_b32 s57, s56
	v_exp_f32_e32 v104, v104
	v_exp_f32_e32 v105, v105
	v_exp_f32_e32 v106, v106
	v_exp_f32_e32 v107, v107
	v_exp_f32_e32 v108, v108
	v_exp_f32_e32 v109, v109
	v_exp_f32_e32 v110, v110
	v_exp_f32_e32 v111, v111
	v_cvt_pk_bf16_f32 v2, v104, v105
	v_cvt_pk_bf16_f32 v3, v106, v107
	v_cvt_pk_bf16_f32 v4, v108, v109
	v_cvt_pk_bf16_f32 v5, v110, v111
	v_add_f32_e32 v82, v104, v105
	v_add_f32_e32 v83, v106, v107
	v_add_f32_e32 v84, v108, v109
	v_add_f32_e32 v85, v110, v111
	v_add_f32_e32 v82, v82, v83
	v_add_f32_e32 v84, v84, v85
	v_add_f32_e32 v82, v82, v84
	v_add_f32_e32 v81, v81, v82
	v_add_f32_e32 v80, v80, v81
	ds_read_b64_tr_b16 v[100:101], v117 offset:0
	ds_read_b64_tr_b16 v[102:103], v117 offset:0x800
	ds_read_b64_tr_b16 v[104:105], v117 offset:0x1000
	ds_read_b64_tr_b16 v[106:107], v117 offset:0x1800
	ds_read_b64_tr_b16 v[108:109], v117 offset:0x2000
	ds_read_b64_tr_b16 v[110:111], v117 offset:0x2800
	ds_read_b64_tr_b16 v[112:113], v117 offset:0x3000
	ds_read_b64_tr_b16 v[114:115], v117 offset:0x3800
	s_waitcnt lgkmcnt(0)
	s_nop 0
	v_mfma_f32_32x32x16_bf16 v[64:79], v[100:103], v[96:99], v[64:79]
	ds_read_b64_tr_b16 v[100:101], v117 offset:0x200
	ds_read_b64_tr_b16 v[102:103], v117 offset:0xa00
	v_mfma_f32_32x32x16_bf16 v[64:79], v[104:107], v[10:13], v[64:79]
	ds_read_b64_tr_b16 v[104:105], v117 offset:0x1200
	ds_read_b64_tr_b16 v[106:107], v117 offset:0x1a00
	v_mfma_f32_32x32x16_bf16 v[64:79], v[108:111], v[6:9], v[64:79]
	ds_read_b64_tr_b16 v[108:109], v117 offset:0x2200
	ds_read_b64_tr_b16 v[110:111], v117 offset:0x2a00
	v_mfma_f32_32x32x16_bf16 v[64:79], v[112:115], v[2:5], v[64:79]
	ds_read_b64_tr_b16 v[112:113], v117 offset:0x3200
	ds_read_b64_tr_b16 v[114:115], v117 offset:0x3a00
	s_waitcnt lgkmcnt(0)
	v_mfma_f32_32x32x16_bf16 v[48:63], v[100:103], v[96:99], v[48:63]
	ds_read_b64_tr_b16 v[100:101], v117 offset:0x400
	ds_read_b64_tr_b16 v[102:103], v117 offset:0xc00
	v_mfma_f32_32x32x16_bf16 v[48:63], v[104:107], v[10:13], v[48:63]
	ds_read_b64_tr_b16 v[104:105], v117 offset:0x1400
	ds_read_b64_tr_b16 v[106:107], v117 offset:0x1c00
	v_mfma_f32_32x32x16_bf16 v[48:63], v[108:111], v[6:9], v[48:63]
	ds_read_b64_tr_b16 v[108:109], v117 offset:0x2400
	ds_read_b64_tr_b16 v[110:111], v117 offset:0x2c00
	v_mfma_f32_32x32x16_bf16 v[48:63], v[112:115], v[2:5], v[48:63]
	ds_read_b64_tr_b16 v[112:113], v117 offset:0x3400
	ds_read_b64_tr_b16 v[114:115], v117 offset:0x3c00
	s_waitcnt lgkmcnt(0)
	v_mfma_f32_32x32x16_bf16 v[32:47], v[100:103], v[96:99], v[32:47]
	ds_read_b64_tr_b16 v[100:101], v117 offset:0x600
	ds_read_b64_tr_b16 v[102:103], v117 offset:0xe00
	v_mfma_f32_32x32x16_bf16 v[32:47], v[104:107], v[10:13], v[32:47]
	ds_read_b64_tr_b16 v[104:105], v117 offset:0x1600
	ds_read_b64_tr_b16 v[106:107], v117 offset:0x1e00
	v_mfma_f32_32x32x16_bf16 v[32:47], v[108:111], v[6:9], v[32:47]
	ds_read_b64_tr_b16 v[108:109], v117 offset:0x2600
	ds_read_b64_tr_b16 v[110:111], v117 offset:0x2e00
	v_mfma_f32_32x32x16_bf16 v[32:47], v[112:115], v[2:5], v[32:47]
	ds_read_b64_tr_b16 v[112:113], v117 offset:0x3600
	ds_read_b64_tr_b16 v[114:115], v117 offset:0x3e00
	s_waitcnt lgkmcnt(0)
	v_mfma_f32_32x32x16_bf16 v[16:31], v[100:103], v[96:99], v[16:31]
	s_mov_b64 s[42:43], 0
	v_mfma_f32_32x32x16_bf16 v[16:31], v[104:107], v[10:13], v[16:31]
	v_mfma_f32_32x32x16_bf16 v[16:31], v[108:111], v[6:9], v[16:31]
	v_mfma_f32_32x32x16_bf16 v[16:31], v[112:115], v[2:5], v[16:31]
	s_mov_b64 s[58:59], -1
	s_and_b64 vcc, exec, s[76:77]
	s_cbranch_vccz .LBB0_833

; #define LAS __attribute__((address_space(3)))
; #define CIN(i) ((const float*)*(const GAS float* const __attribute__((address_space(4)))*)(C.ka + 8 * (i)))
; DI void attn_unit_diff(const Ctx& C, int l, int b, int h, int j) {
;     ...
;     const float inv = 1.f / ol[0];
;     LAS float* cmb = (LAS float*)C.lds + (size_t)wq * (64 * 64);
;     f32x4 sgv[4][4];
;     if (g == 0) { const float* sg0 = CIN(I_SUBLN) + l * 128;
; #pragma unroll
;         for (int d0 = 0; d0 < 4; ++d0)
; #pragma unroll
;             for (int gq = 0; gq < 4; ++gq) sgv[d0][gq] = *(const f32x4*)(sg0 + 32 * d0 + 8 * gq + 4 * hi); }
.LBB0_848:
v_lshlrev_b32_e32 v81, 2, v154
v_xor_b32_e32 v81, 0x80, v81
ds_bpermute_b32 v82, v81, v80
s_waitcnt lgkmcnt(0)
v_add_f32_e32 v80, v80, v82
	v_readlane_b32 s6, v252, 27
	v_readlane_b32 s7, v252, 28
	s_and_b64 vcc, s[6:7], exec
	s_cbranch_vccz .LBB0_850
	s_load_dwordx2 s[6:7], s[0:1], 0x38
	v_readlane_b32 s42, v254, 25
	v_readlane_b32 s43, v254, 26
	s_lshl_b64 s[42:43], s[42:43], 2
	v_lshlrev_b32_e32 v2, 2, v156
	s_waitcnt lgkmcnt(0)
	s_add_u32 s6, s6, s42
	v_ashrrev_i32_e32 v3, 31, v2
	s_addc_u32 s7, s7, s43
	v_lshl_add_u64 v[2:3], v[2:3], 2, s[6:7]
	global_load_dwordx4 v[126:129], v[2:3], off
	global_load_dwordx4 v[94:97], v[2:3], off offset:32
	global_load_dwordx4 v[86:89], v[2:3], off offset:64
	global_load_dwordx4 v[82:85], v[2:3], off offset:96
	global_load_dwordx4 v[90:93], v[2:3], off offset:128
	global_load_dwordx4 v[98:101], v[2:3], off offset:160
	global_load_dwordx4 v[102:105], v[2:3], off offset:192
	global_load_dwordx4 v[106:109], v[2:3], off offset:224
	global_load_dwordx4 v[110:113], v[2:3], off offset:256
	global_load_dwordx4 v[114:117], v[2:3], off offset:288
	global_load_dwordx4 v[118:121], v[2:3], off offset:320
	global_load_dwordx4 v[122:125], v[2:3], off offset:352
	global_load_dwordx4 v[130:133], v[2:3], off offset:384
	global_load_dwordx4 v[10:13], v[2:3], off offset:416
	global_load_dwordx4 v[6:9], v[2:3], off offset:448
	s_nop 0
	global_load_dwordx4 v[2:5], v[2:3], off offset:480
